# static s_setprio 1 for waves 4-7 in every non-GEMM phase (attention, local states, scans, mixer outputs, router, lists, combine); GEMM phases start from priority 0 and keep their per-segment flips
# speedup vs baseline: 1.0070x; 1.0011x over previous
.LBB0_100:
	s_setprio 0
	v_readlane_b32 s8, v252, 1
	v_readlane_b32 s10, v252, 3
	s_cmp_le_i32 s10, s12
	s_cselect_b64 s[6:7], -1, 0
	s_and_b64 s[4:5], s[6:7], s[4:5]
	s_andn2_b64 vcc, exec, s[4:5]
	v_readlane_b32 s9, v252, 2
	v_readlane_b32 s11, v252, 4
	s_cbranch_vccnz .LBB0_153
	v_readlane_b32 s6, v252, 6
	v_mbcnt_lo_u32_b32 v20, -1, 0
	v_mbcnt_hi_u32_b32 v20, -1, v20
	v_readlane_b32 s27, v252, 0
	v_readlane_b32 s7, v252, 7
	s_load_dwordx2 s[46:47], s[6:7], 0xe0
	s_cmpk_gt_i32 s27, 0xff
	s_cbranch_scc1 .LBB0_110
	v_and_b32_e32 v6, 15, v20
	v_ashrrev_i32_e32 v4, 4, v20
	v_lshlrev_b32_e32 v2, 3, v4
	v_lshlrev_b32_e32 v21, 2, v4
	v_lshlrev_b32_e32 v4, 2, v6
	v_mov_b32_e32 v5, v1
	s_waitcnt lgkmcnt(0)
	v_lshl_add_u64 v[4:5], s[46:47], 0, v[4:5]
	s_mov_b64 s[6:7], 0x70200000
	v_ashrrev_i32_e32 v3, 31, v2
	v_lshl_add_u64 v[10:11], v[4:5], 0, s[6:7]
	v_readlane_b32 s6, v254, 9
	v_lshlrev_b32_e32 v0, 12, v6
	v_readlane_b32 s7, v254, 10
	s_add_u32 s6, s46, s6
	v_lshlrev_b64 v[2:3], 1, v[2:3]
	s_addc_u32 s7, s47, s7
	v_lshl_add_u64 v[4:5], v[0:1], 0, v[2:3]
	v_lshl_add_u64 v[12:13], s[6:7], 0, v[4:5]
	v_readlane_b32 s6, v254, 8
	s_add_u32 s6, s46, s6
	v_readlane_b32 s7, v254, 11
	s_addc_u32 s7, s47, s7
	v_lshlrev_b32_e32 v22, 5, v20
	v_lshl_add_u64 v[14:15], s[6:7], 0, v[2:3]
	s_lshl_b32 s6, s27, 6
	v_readlane_b32 s7, v253, 23
	s_or_b32 s6, s7, s6
	v_add_u32_e32 v16, s6, v6
	s_mov_b32 s8, s27
	s_branch .LBB0_104

.LBB0_204:
	s_or_b64 exec, exec, s[4:5]
	s_waitcnt lgkmcnt(0)
	s_barrier
.LBB0_205:
	v_readlane_b32 s100, v252, 5
	s_cmp_ge_u32 s100, 4
	s_cbranch_scc0 .Lprio_done_0
	s_setprio 1
.Lprio_done_0:
	v_readlane_b32 s8, v252, 1
	v_readlane_b32 s10, v252, 3
	s_cmp_le_i32 s10, s12
	s_cselect_b64 s[4:5], -1, 0
	s_and_b64 s[4:5], s[4:5], s[6:7]
	v_writelane_b32 v254, s4, 53
	s_andn2_b64 vcc, exec, s[4:5]
	v_readlane_b32 s9, v252, 2
	v_writelane_b32 v254, s5, 54
	v_readlane_b32 s11, v252, 4
	s_cbranch_vccnz .LBB0_402
	v_readlane_b32 s4, v252, 6
	v_mbcnt_lo_u32_b32 v142, -1, 0
	v_mbcnt_hi_u32_b32 v142, -1, v142
	v_readlane_b32 s27, v252, 0
	v_readlane_b32 s5, v252, 7
	s_load_dwordx2 s[6:7], s[4:5], 0xe0
	s_waitcnt lgkmcnt(0)
	v_writelane_b32 v254, s6, 55
	s_nop 1
	v_writelane_b32 v254, s7, 56
	s_load_dword s6, s[4:5], 0xf0
	s_load_dwordx8 s[40:47], s[4:5], 0x10
	s_waitcnt lgkmcnt(0)
	s_bitcmp0_b32 s6, 0
	v_writelane_b32 v254, s40, 57
	s_nop 1
	v_writelane_b32 v254, s41, 58
	v_writelane_b32 v254, s42, 59
	v_writelane_b32 v254, s43, 60
	v_writelane_b32 v254, s44, 61
	v_writelane_b32 v254, s45, 62
	v_writelane_b32 v254, s46, 63
	v_writelane_b32 v255, s47, 0
	s_load_dwordx8 s[40:47], s[4:5], 0x38
	s_waitcnt lgkmcnt(0)
	v_writelane_b32 v255, s40, 1
	s_nop 1
	v_writelane_b32 v255, s41, 2
	v_writelane_b32 v255, s42, 3
	v_writelane_b32 v255, s43, 4
	v_writelane_b32 v255, s44, 5
	v_writelane_b32 v255, s45, 6
	v_writelane_b32 v255, s46, 7
	v_writelane_b32 v255, s47, 8
	v_writelane_b32 v255, s6, 9
	v_readlane_b32 s6, v252, 10
	s_nop 1
	v_add_u32_e32 v178, s6, v142
	s_cbranch_scc1 .LBB0_284
	v_readlane_b32 s6, v253, 37
	s_cmp_ge_i32 s27, s6
	s_mov_b32 s75, s31
	s_cbranch_scc0 .LBB0_259
	v_readlane_b32 s6, v253, 37
	s_sub_i32 s6, s27, s6
	s_lshl_b32 s10, s6, 3
	v_readlane_b32 s6, v252, 5
	s_add_i32 s10, s10, s6
	s_cmpk_gt_u32 s10, 0xc2ff
	s_cbranch_scc1 .LBB0_259
	s_load_dwordx8 s[40:47], s[4:5], 0x98
	s_load_dwordx4 s[52:55], s[4:5], 0xb8
	s_lshl_b64 s[4:5], s[74:75], 28
	s_mul_i32 s6, s10, 0xaaab
	s_waitcnt lgkmcnt(0)
	s_add_u32 s12, s40, s4
	s_addc_u32 s18, s41, s5
	s_add_u32 s20, s42, s4
	s_addc_u32 s21, s43, s5
	s_add_u32 s48, s44, s4
	s_addc_u32 s49, s45, s5
	s_lshl_b64 s[4:5], s[74:75], 22
	s_add_u32 s50, s46, s4
	s_addc_u32 s51, s47, s5
	s_add_u32 s52, s52, s4
	s_addc_u32 s53, s53, s5
	s_add_u32 s54, s54, s4
	s_addc_u32 s55, s55, s5
	s_lshr_b32 s30, s6, 25
	s_mul_i32 s4, s30, 0x300
	s_sub_i32 s4, s10, s4
	s_and_b32 s11, s4, 0xffff
	s_bfe_u32 s38, s4, 0x80008
	s_cmpk_gt_u32 s11, 0xff
	s_mov_b64 s[4:5], -1
	s_cbranch_scc0 .LBB0_215
	s_cmpk_lt_u32 s10, 0xc000
	s_cselect_b64 s[4:5], -1, 0
	s_lshl_b32 s39, s30, 22
	s_cmp_lg_u32 s38, 1
	s_mov_b64 s[8:9], -1
	s_cbranch_scc0 .LBB0_212
	s_add_u32 s8, s48, s39
	s_addc_u32 s9, s49, 0
	s_and_b64 s[6:7], s[4:5], exec
	s_cselect_b32 s7, s9, s55
	s_cselect_b32 s6, s8, s54
	s_mov_b64 s[8:9], 0

.LBB0_453:
	s_or_b64 exec, exec, s[6:7]
	s_waitcnt lgkmcnt(0)
	s_barrier
.LBB0_454:
	v_readlane_b32 s100, v252, 5
	s_cmp_ge_u32 s100, 4
	s_cbranch_scc0 .Lprio_done_1
	s_setprio 1
.Lprio_done_1:
	v_readlane_b32 s8, v252, 1
	v_readlane_b32 s10, v252, 3
	s_cmp_le_i32 s10, s12
	s_cselect_b64 s[6:7], -1, 0
	s_and_b64 s[4:5], s[6:7], s[4:5]
	s_andn2_b64 vcc, exec, s[4:5]
	v_readlane_b32 s9, v252, 2
	v_readlane_b32 s11, v252, 4
	s_cbranch_vccnz .LBB0_465
	v_mbcnt_lo_u32_b32 v0, -1, 0
	v_mbcnt_hi_u32_b32 v0, -1, v0
	v_readlane_b32 s6, v252, 0
	s_lshl_b32 s6, s6, 9
	v_readlane_b32 s7, v252, 10
	s_add_i32 s6, s6, s7
	v_readlane_b32 s8, v252, 6
	v_add_u32_e32 v0, s6, v0
	s_mov_b32 s6, 0x20000
	v_readlane_b32 s9, v252, 7
	v_cmp_gt_i32_e32 vcc, s6, v0
	s_and_saveexec_b64 s[6:7], vcc
	s_cbranch_execz .LBB0_464
	s_load_dwordx2 s[8:9], s[8:9], 0xe0
	v_lshlrev_b32_e32 v14, 2, v0
	s_mov_b64 s[10:11], 0
	v_mov_b32_e32 v15, v14
	v_mov_b32_e32 v16, v0

.LBB0_516:
	s_or_b64 exec, exec, s[4:5]
	s_waitcnt lgkmcnt(0)
	s_barrier
.LBB0_517:
	v_readlane_b32 s100, v252, 5
	s_cmp_ge_u32 s100, 4
	s_cbranch_scc0 .Lprio_done_2
	s_setprio 1
.Lprio_done_2:
	v_readlane_b32 s8, v252, 1
	v_readlane_b32 s10, v252, 3
	s_cmp_le_i32 s10, s12
	v_readlane_b32 s9, v252, 2
	s_cselect_b64 s[4:5], -1, 0
	s_and_b64 s[8:9], s[4:5], s[6:7]
	s_andn2_b64 vcc, exec, s[8:9]
	v_readlane_b32 s11, v252, 4
	s_cbranch_vccnz .LBB0_656
	v_readlane_b32 s38, v252, 6
	s_waitcnt vmcnt(0)
	v_mbcnt_lo_u32_b32 v184, -1, 0
	v_mbcnt_hi_u32_b32 v184, -1, v184
	v_readlane_b32 s84, v252, 0
	v_readlane_b32 s39, v252, 7
	v_writelane_b32 v254, s74, 55
	v_readlane_b32 s12, v252, 10
	s_nop 0
	v_writelane_b32 v254, s75, 56
	s_load_dwordx8 s[72:79], s[38:39], 0x30
	s_load_dwordx2 s[10:11], s[38:39], 0xe0
	s_load_dword s27, s[38:39], 0xf0
	s_load_dwordx4 s[4:7], s[38:39], 0x50
	s_load_dwordx2 s[48:49], s[38:39], 0x60
	v_add_u32_e32 v185, s12, v184
	s_waitcnt lgkmcnt(0)
	s_bitcmp0_b32 s27, 3
	s_cbranch_scc1 .LBB0_526
	s_cmpk_gt_i32 s84, 0x3ff
	s_cbranch_scc1 .LBB0_526
	s_load_dwordx4 s[40:43], s[38:39], 0x20
	s_add_u32 s50, s10, 0x2a200000
	v_readlane_b32 s38, v254, 55
	s_addc_u32 s51, s11, 0
	v_readlane_b32 s39, v254, 56
	s_add_u32 s52, s10, 0x5a200000
	s_mov_b32 s39, s31
	s_addc_u32 s53, s11, 0
	s_lshl_b64 s[20:21], s[38:39], 15
	s_waitcnt lgkmcnt(0)
	s_add_u32 s54, s40, s20
	s_addc_u32 s55, s41, s21
	s_lshl_b64 s[20:21], s[38:39], 11
	s_add_u32 s56, s42, s20
	s_mov_b32 s12, s38
	s_addc_u32 s57, s43, s21
	v_writelane_b32 v254, s12, 55
	s_lshl_b64 s[20:21], s[38:39], 10
	v_ashrrev_i32_e32 v146, 4, v185
	v_writelane_b32 v254, s13, 56
	s_add_u32 s12, s72, s20
	s_addc_u32 s18, s73, s21
	s_ashr_i32 s20, s84, 8
	s_ashr_i32 s21, s20, 31
	s_lshl_b64 s[38:39], s[20:21], 12
	s_lshl_b32 s20, s84, 6
	s_and_b32 s20, s20, 0xfc0
	s_or_b32 s38, s38, s20
	v_ashrrev_i32_e32 v147, 31, v146
	v_lshl_add_u64 v[2:3], s[38:39], 0, v[146:147]
	v_mov_b64_e32 v[4:5], s[50:51]
	s_movk_i32 s42, 0x4800
	v_mad_u64_u32 v[6:7], s[20:21], v2, s42, v[4:5]
	s_bfe_u32 s40, s84, 0x20006
	v_mad_i32_i24 v7, v3, s42, v7
	v_lshlrev_b32_e32 v3, 3, v185
	s_lshl_b32 s30, s40, 8
	v_and_b32_e32 v2, 0x78, v3
	v_lshlrev_b32_e32 v0, 1, v2
	v_lshl_add_u64 v[6:7], v[6:7], 0, s[30:31]
	v_lshl_add_u64 v[6:7], v[6:7], 0, v[0:1]
	s_movk_i32 s41, 0x1000
	v_add_u32_e32 v10, 0x200, v185
	v_add_co_u32_e32 v6, vcc, s41, v6
	v_ashrrev_i32_e32 v148, 4, v10
	s_nop 0
	v_addc_co_u32_e32 v7, vcc, 0, v7, vcc
	v_ashrrev_i32_e32 v149, 31, v148
	global_load_dwordx4 v[34:37], v[6:7], off offset:2048
	global_load_dwordx4 v[38:41], v[6:7], off offset:3072
	v_lshl_add_u64 v[6:7], s[38:39], 0, v[148:149]
	v_mad_u64_u32 v[8:9], s[20:21], v6, s42, v[4:5]
	v_mad_i32_i24 v9, v7, s42, v9
	v_lshl_add_u64 v[6:7], v[8:9], 0, s[30:31]
	v_lshl_add_u64 v[6:7], v[6:7], 0, v[0:1]
	v_add_co_u32_e32 v6, vcc, s41, v6
	v_ashrrev_i32_e32 v150, 5, v185
	s_nop 0
	v_addc_co_u32_e32 v7, vcc, 0, v7, vcc
	v_ashrrev_i32_e32 v151, 31, v150
	global_load_dwordx4 v[42:45], v[6:7], off offset:2048
	global_load_dwordx4 v[46:49], v[6:7], off offset:3072
	v_lshl_add_u64 v[6:7], s[38:39], 0, v[150:151]
	v_mad_u64_u32 v[8:9], s[20:21], v6, s42, v[4:5]
	v_ashrrev_i32_e32 v152, 5, v10
	v_mad_i32_i24 v9, v7, s42, v9
	s_lshl_b32 s30, s40, 9
	v_ashrrev_i32_e32 v153, 31, v152
	v_lshl_add_u64 v[6:7], v[8:9], 0, s[30:31]
	v_and_b32_e32 v8, 0xf8, v3
	v_lshl_add_u64 v[10:11], s[38:39], 0, v[152:153]
	v_lshlrev_b32_e32 v0, 1, v8
	v_mad_u64_u32 v[12:13], s[20:21], v10, s42, v[4:5]
	v_lshl_add_u64 v[6:7], v[6:7], 0, v[0:1]
	s_movk_i32 s40, 0x2000
	v_mad_i32_i24 v13, v11, s42, v13
	v_add_co_u32_e32 v6, vcc, s40, v6
	v_lshl_add_u64 v[10:11], v[12:13], 0, s[30:31]
	v_add_u32_e32 v3, 0x400, v185
	v_addc_co_u32_e32 v7, vcc, 0, v7, vcc
	v_lshl_add_u64 v[10:11], v[10:11], 0, v[0:1]
	v_ashrrev_i32_e32 v154, 5, v3
	v_add_co_u32_e32 v10, vcc, s40, v10
	v_ashrrev_i32_e32 v155, 31, v154
	s_nop 0
	v_addc_co_u32_e32 v11, vcc, 0, v11, vcc
	global_load_dwordx4 v[82:85], v[6:7], off
	global_load_dwordx4 v[86:89], v[10:11], off
	v_lshl_add_u64 v[6:7], s[38:39], 0, v[154:155]
	v_add_u32_e32 v3, 0x600, v185
	v_mad_u64_u32 v[10:11], s[20:21], v6, s42, v[4:5]
	v_ashrrev_i32_e32 v156, 5, v3
	v_mad_i32_i24 v11, v7, s42, v11
	v_ashrrev_i32_e32 v157, 31, v156
	v_lshl_add_u64 v[6:7], v[10:11], 0, s[30:31]
	v_lshl_add_u64 v[10:11], s[38:39], 0, v[156:157]
	v_mad_u64_u32 v[4:5], s[20:21], v10, s42, v[4:5]
	v_lshl_add_u64 v[6:7], v[6:7], 0, v[0:1]
	v_mad_i32_i24 v5, v11, s42, v5
	v_add_co_u32_e32 v6, vcc, s40, v6
	v_lshl_add_u64 v[4:5], v[4:5], 0, s[30:31]
	s_nop 0
	v_addc_co_u32_e32 v7, vcc, 0, v7, vcc
	v_lshl_add_u64 v[4:5], v[4:5], 0, v[0:1]
	v_add_co_u32_e32 v4, vcc, s40, v4
	v_and_b32_e32 v0, 15, v184
	s_nop 0
	v_addc_co_u32_e32 v5, vcc, 0, v5, vcc
	global_load_dwordx4 v[90:93], v[6:7], off
	global_load_dwordx4 v[94:97], v[4:5], off
	v_lshlrev_b32_e32 v4, 2, v146
	v_and_b32_e32 v4, 12, v4
	v_bfe_u32 v5, v146, 2, 2
	v_bitop3_b32 v4, v4, v0, v5 bitop3:0x36
	v_lshlrev_b32_e32 v5, 2, v148
	v_lshlrev_b32_e32 v3, 8, v146
	v_and_b32_e32 v5, 12, v5
	v_bfe_u32 v6, v148, 2, 2
	v_lshl_or_b32 v3, v4, 4, v3
	v_lshlrev_b32_e32 v4, 8, v148
	v_bitop3_b32 v5, v5, v0, v6 bitop3:0x36
	v_lshl_or_b32 v6, v5, 4, v4
	v_lshlrev_b32_e32 v4, 10, v184
	v_lshlrev_b32_e32 v5, 2, v150
	v_and_b32_e32 v4, 0x4000, v4
	v_and_b32_e32 v5, 12, v5
	v_bfe_u32 v9, v150, 2, 2
	v_add_u32_e32 v4, 0, v4
	v_bitop3_b32 v5, v5, v0, v9 bitop3:0x36
	v_lshl_add_u32 v9, v5, 4, v4
	v_lshlrev_b32_e32 v5, 2, v152
	v_and_b32_e32 v5, 12, v5
	v_bfe_u32 v11, v152, 2, 2
	v_bitop3_b32 v5, v5, v0, v11 bitop3:0x36
	v_lshl_add_u32 v11, v5, 4, v4
	v_lshlrev_b32_e32 v5, 2, v154
	v_and_b32_e32 v5, 12, v5
	v_bfe_u32 v13, v154, 2, 2
	v_bitop3_b32 v5, v5, v0, v13 bitop3:0x36
	v_lshl_add_u32 v13, v5, 4, v4
	v_lshlrev_b32_e32 v5, 2, v156
	s_lshl_b64 s[20:21], s[90:91], 2
	v_and_b32_e32 v5, 12, v5
	v_bfe_u32 v15, v156, 2, 2
	s_add_u32 s58, s12, s20
	v_bitop3_b32 v5, v5, v0, v15 bitop3:0x36
	v_lshlrev_b32_e32 v0, 2, v0
	s_addc_u32 s59, s18, s21
	v_lshlrev_b32_e32 v7, 8, v150
	v_lshlrev_b32_e32 v10, 8, v152
	v_lshlrev_b32_e32 v12, 8, v154
	v_lshlrev_b32_e32 v14, 8, v156
	v_lshl_add_u32 v15, v5, 4, v4
	v_and_b32_e32 v186, 0x7f, v185
	v_lshl_add_u64 v[4:5], s[10:11], 0, v[0:1]
	s_mov_b64 s[20:21], 0x70200000
	v_readlane_b32 s12, v253, 45
	v_ashrrev_i32_e32 v0, 7, v185
	v_lshl_add_u64 v[158:159], v[4:5], 0, s[20:21]
	v_lshl_add_u32 v187, v184, 2, s12
	v_lshl_add_u32 v188, v0, 10, 0
	v_lshl_add_u32 v189, v186, 2, 0
	v_cmp_lt_i32_e64 s[38:39], 0, v0
	v_cmp_lt_i32_e64 s[40:41], 1, v0
	v_cmp_lt_i32_e64 s[42:43], 2, v0
	v_cmp_lt_i32_e64 s[44:45], 3, v0
	v_add_u32_e32 v190, 0, v3
	v_add_u32_e32 v191, 0, v6
	v_add_u32_e32 v192, v9, v7
	v_add_u32_e32 v193, v11, v10
	v_add_u32_e32 v194, v13, v12
	v_add_u32_e32 v195, v15, v14
	v_lshlrev_b32_e32 v160, 1, v2
	v_lshlrev_b32_e32 v162, 1, v8
	s_mov_b32 s12, s84
	s_branch .LBB0_522

.LBB0_708:
	s_setprio 0
	v_readlane_b32 s8, v252, 1
	v_readlane_b32 s10, v252, 3
	s_cmp_le_i32 s10, s12
	s_cselect_b64 s[6:7], -1, 0
	s_and_b64 s[4:5], s[6:7], s[4:5]
	s_mov_b32 s6, s74
	v_writelane_b32 v254, s6, 55
	s_andn2_b64 vcc, exec, s[4:5]
	v_readlane_b32 s9, v252, 2
	v_writelane_b32 v254, s7, 56
	v_readlane_b32 s11, v252, 4
	s_cbranch_vccnz .LBB0_742
	v_mbcnt_lo_u32_b32 v0, -1, 0
	v_mbcnt_hi_u32_b32 v0, -1, v0
	v_readlane_b32 s27, v252, 0
	v_readlane_b32 s6, v252, 10
	s_movk_i32 s38, 0xc00
	s_cmpk_gt_i32 s27, 0x1ff
	v_add_u32_e32 v0, s6, v0
	v_readlane_b32 s6, v252, 6
	v_readlane_b32 s7, v252, 7
	s_nop 0
	v_readfirstlane_b32 s18, v0
	s_cbranch_scc1 .LBB0_742
	s_ashr_i32 s64, s27, 31
	s_lshr_b32 s8, s64, 29
	s_add_i32 s11, s27, s8
	s_and_b32 s8, s11, -8
	s_sub_i32 s10, s27, s8
	s_cmp_gt_i32 s10, -1
	s_mov_b64 s[8:9], -1
	s_cbranch_scc0 .LBB0_712
	s_lshl_b32 s12, s10, 6
	s_mov_b64 s[8:9], 0

.LBB0_794:
	s_setprio 0
	v_readlane_b32 s8, v252, 1
	v_readlane_b32 s10, v252, 3
	s_cmp_le_i32 s10, s12
	s_cselect_b64 s[4:5], -1, 0
	s_and_b64 s[4:5], s[4:5], s[6:7]
	s_andn2_b64 vcc, exec, s[4:5]
	v_readlane_b32 s9, v252, 2
	v_readlane_b32 s11, v252, 4
	s_cbranch_vccnz .LBB0_824
	v_mbcnt_lo_u32_b32 v0, -1, 0
	v_mbcnt_hi_u32_b32 v0, -1, v0
	v_readlane_b32 s20, v252, 0
	v_readlane_b32 s6, v252, 10
	s_movk_i32 s38, 0x800
	s_cmpk_gt_i32 s20, 0x1ff
	v_add_u32_e32 v16, s6, v0
	v_readlane_b32 s6, v252, 6
	v_readlane_b32 s7, v252, 7
	s_nop 0
	v_readfirstlane_b32 s50, v16
	s_cbranch_scc1 .LBB0_824
	s_ashr_i32 s21, s20, 31
	s_lshr_b32 s8, s21, 29
	s_add_i32 s11, s20, s8
	s_and_b32 s8, s11, -8
	s_sub_i32 s10, s20, s8
	s_cmp_gt_i32 s10, -1
	s_mov_b64 s[8:9], -1
	s_cbranch_scc0 .LBB0_798
	s_lshl_b32 s12, s10, 6
	s_mov_b64 s[8:9], 0

.LBB0_875:
	s_or_b64 exec, exec, s[4:5]
	s_waitcnt lgkmcnt(0)
	s_barrier
.LBB0_876:
	v_readlane_b32 s100, v252, 5
	s_cmp_ge_u32 s100, 4
	s_cbranch_scc0 .Lprio_done_3
	s_setprio 1
.Lprio_done_3:
	v_readlane_b32 s4, v254, 50
	v_readlane_b32 s8, v252, 1
	s_add_i32 s6, s4, 8
	v_readlane_b32 s10, v252, 3
	v_readlane_b32 s11, v252, 4
	s_cmp_le_i32 s10, s6
	s_cselect_b64 s[4:5], -1, 0
	s_cmp_lt_i32 s6, s11
	v_readlane_b32 s9, v252, 2
	s_cselect_b64 s[6:7], -1, 0
	s_and_b64 s[8:9], s[4:5], s[6:7]
	s_andn2_b64 vcc, exec, s[8:9]
	s_cbranch_vccnz .LBB0_896
	s_waitcnt vmcnt(0)
	v_mbcnt_lo_u32_b32 v66, -1, 0
	v_mbcnt_hi_u32_b32 v66, -1, v66
	v_readlane_b32 s27, v252, 0
	v_readlane_b32 s10, v252, 6
	v_readlane_b32 s11, v252, 7
	s_cmpk_gt_i32 s27, 0xff
	s_cbranch_scc1 .LBB0_896
	v_readlane_b32 s4, v252, 10
	s_load_dwordx2 s[58:59], s[10:11], 0xe0
	v_lshl_add_u32 v2, s74, 6, v66
	v_add_u32_e32 v71, s4, v66
	s_load_dwordx4 s[4:7], s[10:11], 0x78
	s_load_dwordx2 s[20:21], s[10:11], 0x90
	v_ashrrev_i32_e32 v3, 31, v2
	s_waitcnt lgkmcnt(0)
	s_add_u32 s66, s58, 0x100000
	s_addc_u32 s67, s59, 0
	s_add_u32 s68, s58, 0x140000
	v_lshl_add_u64 v[2:3], v[2:3], 2, s[20:21]
	global_load_dword v112, v[2:3], off
	s_addc_u32 s69, s59, 0
	v_and_b32_e32 v0, 15, v66
	s_add_u32 s10, s58, 0x200000
	v_ashrrev_i32_e32 v6, 4, v66
	v_lshlrev_b64 v[4:5], v66, -1
	v_readlane_b32 s18, v253, 43
	s_addc_u32 s11, s59, 0
	s_lshl_b32 s30, s74, 11
	v_lshlrev_b32_e32 v7, 2, v0
	v_not_b32_e32 v70, v4
	v_lshl_add_u32 v4, v6, 10, s18
	s_add_i32 s12, 0, 0x20000
	v_add3_u32 v116, 0, v7, v4
	s_lshl_b64 s[20:21], s[30:31], 2
	v_lshlrev_b32_e32 v4, 1, v66
	v_not_b32_e32 v69, v5
	s_add_u32 s4, s4, s20
	v_ashrrev_i32_e32 v5, 31, v4
	s_addc_u32 s5, s5, s21
	v_lshlrev_b64 v[4:5], 4, v[4:5]
	v_lshl_add_u64 v[72:73], s[4:5], 0, v[4:5]
	s_add_u32 s4, s6, s20
	s_addc_u32 s5, s7, s21
	v_lshl_add_u64 v[74:75], s[4:5], 0, v[4:5]
	s_mov_b64 s[4:5], 0x1800
	v_lshlrev_b32_e32 v8, 2, v66
	v_readlane_b32 s60, v254, 34
	v_lshl_add_u64 v[80:81], v[72:73], 0, s[4:5]
	v_lshl_add_u64 v[82:83], v[74:75], 0, s[4:5]
	v_ashrrev_i32_e32 v67, 31, v66
	v_lshlrev_b32_e32 v4, 2, v71
	v_readlane_b32 s4, v253, 45
	v_add_u32_e32 v117, s60, v4
	v_add_u32_e32 v123, s12, v4
	v_add_u32_e32 v118, s4, v8
	v_lshl_add_u64 v[4:5], v[66:67], 4, s[58:59]
	s_mov_b64 s[4:5], 0x68200000
	v_lshl_add_u64 v[84:85], v[4:5], 0, s[4:5]
	v_lshl_add_u64 v[4:5], v[66:67], 3, s[58:59]
	s_mov_b64 s[4:5], 0x64200000
	v_lshlrev_b32_e32 v2, 3, v6
	v_lshl_add_u64 v[86:87], v[4:5], 0, s[4:5]
	v_readlane_b32 s4, v254, 15
	v_ashrrev_i32_e32 v3, 31, v2
	v_readlane_b32 s5, v254, 16
	s_add_u32 s4, s58, s4
	s_addc_u32 s5, s59, s5
	v_lshlrev_b64 v[2:3], 1, v[2:3]
	v_lshl_or_b32 v90, s27, 6, v0
	v_lshlrev_b32_e32 v0, 12, v0
	v_ashrrev_i32_e32 v9, 3, v66
	v_lshl_add_u64 v[88:89], s[4:5], 0, v[2:3]
	v_lshl_add_u64 v[2:3], v[0:1], 0, v[2:3]
	v_add_u32_e32 v113, s12, v8
	v_and_b32_e32 v68, -8, v66
	v_and_b32_e32 v114, 7, v66
	v_cmp_eq_u32_e64 s[38:39], 0, v66
	v_add_u32_e32 v115, s60, v8
	v_cmp_lt_i32_e64 s[40:41], 0, v9
	v_cmp_lt_i32_e64 s[42:43], 1, v9
	v_cmp_lt_i32_e64 s[44:45], 2, v9
	v_cmp_lt_i32_e64 s[46:47], 3, v9
	v_cmp_lt_i32_e64 s[48:49], 4, v9
	v_cmp_lt_i32_e64 s[50:51], 5, v9
	v_cmp_lt_i32_e64 s[52:53], 6, v9
	v_cmp_lt_i32_e64 s[54:55], 7, v9
	v_lshl_add_u64 v[76:77], v[72:73], 0, s[0:1]
	v_lshl_add_u64 v[78:79], v[74:75], 0, s[0:1]
	v_cmp_gt_i32_e64 s[56:57], 64, v71
	v_add_u32_e32 v119, 0x10000, v118
	v_add_u32_e32 v120, 0x14000, v118
	v_add_u32_e32 v121, 0x18000, v118
	v_add_u32_e32 v122, 0x1c000, v118
	v_add_u32_e32 v124, 0x10800, v118
	v_add_u32_e32 v125, 0x14800, v118
	v_add_u32_e32 v126, 0x18800, v118
	v_add_u32_e32 v127, 0x1c800, v118
	v_add_u32_e32 v128, 0x800, v123
	v_add_u32_e32 v129, 0x11000, v118
	v_add_u32_e32 v130, 0x15000, v118
	v_add_u32_e32 v131, 0x19000, v118
	v_add_u32_e32 v132, 0x1d000, v118
	v_add_u32_e32 v133, 0x1000, v123
	v_add_u32_e32 v134, 0x11800, v118
	v_add_u32_e32 v135, 0x15800, v118
	v_add_u32_e32 v136, 0x19800, v118
	v_add_u32_e32 v137, 0x1d800, v118
	v_add_u32_e32 v138, 0x1800, v123
	v_add_u32_e32 v139, 0x12000, v118
	v_add_u32_e32 v140, 0x16000, v118
	v_add_u32_e32 v141, 0x1a000, v118
	v_add_u32_e32 v142, 0x1e000, v118
	v_add_u32_e32 v143, 0x2000, v123
	v_add_u32_e32 v144, 0x12800, v118
	v_add_u32_e32 v145, 0x16800, v118
	v_add_u32_e32 v146, 0x1a800, v118
	v_add_u32_e32 v147, 0x1e800, v118
	v_add_u32_e32 v148, 0x2800, v123
	v_add_u32_e32 v149, 0x13000, v118
	v_add_u32_e32 v150, 0x17000, v118
	v_add_u32_e32 v151, 0x1b000, v118
	v_add_u32_e32 v152, 0x1f000, v118
	v_add_u32_e32 v153, 0x3000, v123
	v_add_u32_e32 v154, 0x13800, v118
	v_add_u32_e32 v155, 0x17800, v118
	v_add_u32_e32 v156, 0x1b800, v118
	v_add_u32_e32 v157, 0x1f800, v118
	v_add_u32_e32 v158, 0x3800, v123
	v_lshl_add_u64 v[92:93], s[4:5], 0, v[2:3]
	s_branch .LBB0_880

.LBB0_947:
	s_or_b64 exec, exec, s[6:7]
	s_waitcnt lgkmcnt(0)
	s_barrier
.LBB0_948:
	v_readlane_b32 s100, v252, 5
	s_cmp_ge_u32 s100, 4
	s_cbranch_scc0 .Lprio_done_4
	s_setprio 1
.Lprio_done_4:
	v_readlane_b32 s8, v252, 1
	v_readlane_b32 s10, v252, 3
	s_cmp_le_i32 s10, s12
	s_cselect_b64 s[6:7], -1, 0
	s_and_b64 s[4:5], s[6:7], s[4:5]
	s_andn2_b64 vcc, exec, s[4:5]
	v_readlane_b32 s9, v252, 2
	v_readlane_b32 s11, v252, 4
	s_cbranch_vccnz .LBB0_1018
	v_mbcnt_lo_u32_b32 v10, -1, 0
	v_mbcnt_hi_u32_b32 v10, -1, v10
	v_readlane_b32 s12, v252, 0
	v_readlane_b32 s6, v252, 6
	v_readlane_b32 s7, v252, 7
	s_cmpk_gt_i32 s12, 0xff
	s_cbranch_scc1 .LBB0_1018
	s_load_dwordx2 s[64:65], s[6:7], 0xe0
	v_readlane_b32 s6, v252, 10
	v_and_b32_e32 v0, 63, v10
	v_lshl_add_u32 v19, v0, 2, 0
	v_add_u32_e32 v2, s6, v10
	v_and_b32_e32 v3, 0x3fffffc0, v2
	v_ashrrev_i32_e32 v4, 6, v2
	s_movk_i32 s6, 0x100
	v_lshl_add_u32 v20, v3, 2, v19
	v_max_i32_e32 v3, 0xfffffe40, v2
	v_cmp_gt_i32_e64 s[38:39], s6, v4
	s_waitcnt lgkmcnt(0)
	s_add_u32 s6, s64, 0x100000
	v_sub_u32_e32 v3, v3, v2
	s_addc_u32 s7, s65, 0
	v_lshlrev_b32_e32 v5, 2, v10
	v_readlane_b32 s18, v253, 45
	v_add_u32_e32 v3, 0x1ff, v3
	s_add_u32 s8, s64, 0x200000
	v_add_u32_e32 v18, s18, v5
	v_add_u32_e32 v21, -4, v5
	v_add_u32_e32 v22, -8, v5
	v_add_u32_e32 v23, -16, v5
	v_subrev_u32_e32 v24, 32, v5
	v_subrev_u32_e32 v25, 64, v5
	v_add_u32_e32 v26, 0xffffff80, v5
	v_add_u32_e32 v27, 0, v5
	v_lshrrev_b32_e32 v5, 9, v3
	s_addc_u32 s9, s65, 0
	v_add_u32_e32 v12, 1, v5
	v_max_i32_e32 v5, 0xf8, v4
	s_add_u32 s10, s64, 0x240000
	v_sub_u32_e32 v5, v5, v4
	s_addc_u32 s11, s65, 0
	v_add_u32_e32 v5, 7, v5
	s_add_u32 s66, s64, 0x300000
	v_lshrrev_b32_e32 v11, 3, v5
	s_addc_u32 s67, s65, 0
	v_add_u32_e32 v13, 1, v11
	s_movk_i32 s18, 0x67
	v_lshlrev_b32_e32 v11, 6, v5
	s_add_u32 s68, s64, 0x400000
	v_cmp_lt_u32_e32 vcc, s18, v5
	v_and_b32_e32 v11, 0xfffffe00, v11
	s_mov_b32 s18, 0x3ffffff
	s_addc_u32 s69, s65, 0
	v_cmp_lt_u32_e64 s[58:59], s18, v5
	v_add_u32_e32 v5, v2, v11
	s_add_u32 s72, s64, 0x401000
	v_cmp_lt_i32_e64 s[60:61], v5, v2
	s_addc_u32 s73, s65, 0
	s_or_b64 s[20:21], s[60:61], s[58:59]
	s_xor_b64 s[20:21], s[20:21], -1
	s_movk_i32 s18, 0x1ff
	v_cmp_lt_u32_e64 s[60:61], s18, v3
	s_and_b64 s[74:75], vcc, s[20:21]
	s_lshl_b32 s18, s12, 6
	s_lshl_b32 s20, s12, 9
	v_lshlrev_b64 v[8:9], v10, -1
	v_and_b32_e32 v30, 0x3ffffffe, v13
	v_and_b32_e32 v32, 0xfffffe, v12
	s_add_u32 s76, s64, 0x400900
	v_cmp_lt_i32_e64 s[40:41], 0, v10
	v_cmp_gt_i32_e64 s[42:43], 2, v10
	v_cmp_gt_i32_e64 s[44:45], 4, v10
	v_cmp_gt_i32_e64 s[46:47], 8, v10
	v_cmp_gt_i32_e64 s[48:49], 16, v10
	v_cmp_gt_i32_e64 s[50:51], 32, v10
	v_cmp_eq_u32_e64 s[52:53], 63, v0
	v_lshlrev_b64 v[6:7], v10, 1
	v_not_b32_e32 v9, v9
	v_not_b32_e32 v8, v8
	v_cmp_gt_i32_e64 s[54:55], 64, v2
	v_cmp_eq_u32_e64 s[56:57], 0, v2
	v_not_b32_e32 v28, v10
	v_add_u32_e32 v29, 64, v10
	v_lshl_add_u32 v31, v30, 3, v4
	v_mov_b32_e32 v11, v0
	v_add_u32_e32 v5, 8, v4
	v_cmp_ne_u32_e64 s[58:59], v13, v30
	v_lshl_add_u32 v33, v32, 9, v2
	v_add_u32_e32 v3, 0x200, v2
	v_cmp_ne_u32_e64 s[62:63], v12, v32
	s_addc_u32 s77, s65, 0
	s_add_i32 s78, s18, 0x24000
	s_branch .LBB0_952

.LBB0_1070:
	s_setprio 0
	v_readlane_b32 s8, v252, 1
	v_readlane_b32 s10, v252, 3
	s_cmp_le_i32 s10, s12
	s_cselect_b64 s[4:5], -1, 0
	s_and_b64 s[4:5], s[4:5], s[6:7]
	s_andn2_b64 vcc, exec, s[4:5]
	v_readlane_b32 s9, v252, 2
	v_readlane_b32 s11, v252, 4
	s_cbranch_vccnz .LBB0_1203
	v_readlane_b32 s6, v252, 6
	v_mbcnt_lo_u32_b32 v0, -1, 0
	v_mbcnt_hi_u32_b32 v0, -1, v0
	v_readlane_b32 s20, v252, 0
	v_readlane_b32 s7, v252, 7
	s_load_dwordx2 s[48:49], s[6:7], 0xe0
	v_mov_b32_e32 v2, 0x401000
	s_and_b32 s6, s20, 7
	s_ashr_i32 s18, s20, 3
	s_ashr_i32 s7, s20, 31
	s_waitcnt lgkmcnt(0)
	global_load_dword v2, v2, s[48:49]
	v_readlane_b32 s8, v253, 60
	s_mul_i32 s21, s6, s8
	s_lshr_b32 s6, s18, 30
	s_lshr_b32 s7, s7, 30
	s_add_i32 s12, s18, s6
	s_add_i32 s6, s20, s7
	s_ashr_i32 s54, s12, 2
	s_ashr_i32 s46, s6, 2
	v_readlane_b32 s6, v253, 56
	s_add_i32 s21, s21, s54
	v_readlane_b32 s7, v253, 57
	s_waitcnt vmcnt(0)
	v_readfirstlane_b32 s27, v2
	s_add_i32 s30, s27, 64
	s_and_b64 s[6:7], s[6:7], exec
	s_cselect_b32 s6, s21, s46
	v_readlane_b32 s7, v252, 10
	s_cmp_ge_i32 s6, s30
	s_nop 0
	v_add_u32_e32 v0, s7, v0
	s_cbranch_scc1 .LBB0_1176
	s_add_u32 s44, s48, 0x400000
	s_addc_u32 s45, s49, 0
	s_sub_i32 s7, s6, s27
	s_addk_i32 s7, 0x240
	s_cmp_lt_i32 s6, s27
	v_cmp_eq_u32_e64 s[38:39], 0, v0
	s_cselect_b32 s8, s6, s7
	s_and_saveexec_b64 s[6:7], s[38:39]
	s_cbranch_execz .LBB0_1074
	s_ashr_i32 s9, s8, 31
	s_lshl_b64 s[10:11], s[8:9], 2
	s_add_u32 s10, s44, s10
	s_addc_u32 s11, s45, s11
	global_load_dword v64, v1, s[10:11]
	s_add_i32 s9, 0, 0x23000
	v_mov_b32_e32 v3, s9

.LBB0_1255:
	s_setprio 0
	v_readlane_b32 s8, v252, 1
	v_readlane_b32 s10, v252, 3
	s_cmp_le_i32 s10, s12
	s_cselect_b64 s[4:5], -1, 0
	s_and_b64 s[4:5], s[4:5], s[6:7]
	s_andn2_b64 vcc, exec, s[4:5]
	v_readlane_b32 s9, v252, 2
	v_readlane_b32 s11, v252, 4
	s_cbranch_vccnz .LBB0_1298
	v_mbcnt_lo_u32_b32 v0, -1, 0
	v_mbcnt_hi_u32_b32 v0, -1, v0
	v_readlane_b32 s20, v252, 0
	v_readlane_b32 s6, v252, 10
	s_mov_b32 s10, 0
	s_mov_b32 s11, s20
	v_add_u32_e32 v14, s6, v0
	v_readlane_b32 s6, v252, 6
	v_readlane_b32 s7, v252, 7
	s_load_dwordx2 s[44:45], s[6:7], 0xe0
	v_mov_b32_e32 v0, 0x401000
	v_readlane_b32 s7, v253, 60
	v_cmp_eq_u32_e64 s[38:39], 0, v14
	s_waitcnt lgkmcnt(0)
	global_load_dword v0, v0, s[44:45]
	s_add_u32 s8, s44, 0x400000
	s_addc_u32 s9, s45, 0
	s_and_b32 s6, s20, 7
	s_mul_i32 s30, s6, s7
	s_ashr_i32 s6, s20, 5
	s_add_i32 s30, s30, s6
	s_mov_b32 s12, s30
	s_waitcnt vmcnt(0)
	v_readfirstlane_b32 s21, v0
	s_add_i32 s27, s21, 64
	s_mov_b32 s100, 0
	s_branch .LBB0_1259

.LBB0_1350:
	s_or_b64 exec, exec, s[4:5]
	s_waitcnt lgkmcnt(0)
	s_barrier
.LBB0_1351:
	v_readlane_b32 s100, v252, 5
	s_cmp_ge_u32 s100, 4
	s_cbranch_scc0 .Lprio_done_5
	s_setprio 1
.Lprio_done_5:
	v_readlane_b32 s4, v254, 47
	v_readlane_b32 s5, v254, 48
	v_readlane_b32 s8, v252, 1
	s_xor_b64 s[40:41], s[4:5], -1
	v_readlane_b32 s10, v252, 3
	s_cmp_le_i32 s10, s12
	s_cselect_b64 s[4:5], -1, 0
	s_and_b64 s[42:43], s[4:5], s[6:7]
	s_andn2_b64 vcc, exec, s[42:43]
	v_readlane_b32 s9, v252, 2
	v_readlane_b32 s11, v252, 4
	s_cbranch_vccnz .LBB0_1371
	v_mbcnt_lo_u32_b32 v61, -1, 0
	v_mbcnt_hi_u32_b32 v61, -1, v61
	v_readlane_b32 s27, v252, 0
	s_lshl_b32 s4, s27, 3
	v_readlane_b32 s5, v252, 5
	v_readlane_b32 s38, v252, 6
	s_add_i32 s44, s4, s5
	v_readlane_b32 s39, v252, 7
	s_cmpk_gt_i32 s44, 0x3fff
	s_cbranch_scc1 .LBB0_1371
	s_load_dwordx8 s[4:11], s[38:39], 0xc8
	v_readlane_b32 s38, v254, 47
	v_readlane_b32 s39, v254, 48
	s_waitcnt lgkmcnt(0)
	s_add_u32 s46, s10, 0x2a200000
	s_addc_u32 s47, s11, 0
	s_add_u32 s12, s10, 0x240000
	s_addc_u32 s18, s11, 0
	s_add_u32 s20, s10, 0x140000
	s_addc_u32 s21, s11, 0
	s_add_u32 s30, s10, 0x22200000
	s_addc_u32 s45, s11, 0
	s_and_b64 s[38:39], s[38:39], exec
	s_cselect_b32 s9, s45, s9
	s_cselect_b32 s8, s30, s8
	s_lshl_b32 s30, s74, 11
	s_lshl_b64 s[38:39], s[30:31], 2
	s_add_u32 s4, s4, s38
	s_addc_u32 s5, s5, s39
	s_add_u32 s6, s6, s38
	s_addc_u32 s7, s7, s39
	s_ashr_i32 s45, s44, 31
	s_lshl_b32 s27, s27, 6
	v_readlane_b32 s30, v254, 30
	s_lshl_b64 s[48:49], s[44:45], 11
	s_add_i32 s50, s30, s27
	s_lshl_b64 s[52:53], s[44:45], 12
	s_lshl_b64 s[54:55], s[44:45], 13
	s_add_i32 s100, s50, -7
	s_lshl_b32 s100, s100, 2
	v_mov_b32_e32 v60, s100
	v_add_u32_e32 v94, 0x100000, v60
	global_load_dwordx4 v[194:197], v94, s[20:21]
	global_load_dwordx4 v[198:201], v94, s[20:21] offset:16
	global_load_dwordx4 v[202:205], v60, s[20:21]
	global_load_dwordx4 v[206:209], v60, s[20:21] offset:16
	s_waitcnt vmcnt(0)
	s_branch .LBB0_1355
